# gemm3 layer-0 residual epilogue software-pipelined (32 row loads through a rolling window instead of 8 serial batches)
# speedup vs baseline: 1.0125x; 1.0125x over previous
.LBB0_705:
	s_lshl_b64 s[48:49], s[48:49], 12
	v_readlane_b32 s4, v252, 45
	v_readlane_b32 s5, v252, 46
	s_add_u32 s48, s4, s48
	s_addc_u32 s49, s5, s49
	s_lshl_b64 s[50:51], s[50:51], 2
	s_add_u32 s50, s53, s50
	s_addc_u32 s51, s55, s51
	s_lshl_b32 s15, s42, 8
	v_readlane_b32 s4, v255, 47
	s_or_b32 s15, s15, s4
	v_lshl_add_u32 v184, v175, 2, s15
	v_readlane_b32 s4, v255, 51
	v_lshlrev_b32_e32 v185, 2, v184
	s_nop 1
	v_add_u32_e32 v186, s4, v5
	v_readlane_b32 s4, v255, 43
	v_readlane_b32 s5, v255, 44
	v_lshl_add_u32 v176, v186, 13, v185
	v_add_u32_e32 v177, 0x20000, v176
	v_add_u32_e32 v178, 0x40000, v176
	v_add_u32_e32 v179, 0x60000, v176
	v_add_u32_e32 v180, 0x100000, v176
	v_add_u32_e32 v181, 0x120000, v176
	v_add_u32_e32 v182, 0x140000, v176
	v_add_u32_e32 v183, 0x160000, v176
	global_load_dwordx4 v[8:11], v185, s[50:51]
	global_load_dwordx4 v[24:27], v185, s[4:5]
	global_load_dwordx4 v[12:15], v185, s[50:51] offset:64
	global_load_dwordx4 v[28:31], v185, s[4:5] offset:64
	global_load_dwordx4 v[16:19], v185, s[50:51] offset:512
	global_load_dwordx4 v[32:35], v185, s[4:5] offset:512
	global_load_dwordx4 v[20:23], v185, s[50:51] offset:576
	global_load_dwordx4 v[192:195], v185, s[4:5] offset:576
	global_load_dwordx4 v[196:199], v176, s[46:47]
	global_load_dwordx4 v[216:219], v176, s[46:47] offset:64
	global_load_dwordx4 v[220:223], v177, s[46:47]
	global_load_dwordx4 v[224:227], v177, s[46:47] offset:64
	global_load_dwordx4 v[228:231], v178, s[46:47]
	global_load_dwordx4 v[232:235], v178, s[46:47] offset:64
	global_load_dwordx4 v[236:239], v179, s[46:47]
	s_mov_b32 s4, 0x37800000
	s_mov_b64 s[42:43], -1
	s_waitcnt vmcnt(7)
	v_pk_add_f32 v[8:9], v[8:9], v[24:25]
	v_pk_add_f32 v[10:11], v[10:11], v[26:27]
	v_pk_mul_f32 v[8:9], v[8:9], s[4:5] op_sel_hi:[1,0]
	v_pk_mul_f32 v[10:11], v[10:11], s[4:5] op_sel_hi:[1,0]
	v_pk_add_f32 v[12:13], v[12:13], v[28:29]
	v_pk_add_f32 v[14:15], v[14:15], v[30:31]
	v_pk_mul_f32 v[12:13], v[12:13], s[4:5] op_sel_hi:[1,0]
	v_pk_mul_f32 v[14:15], v[14:15], s[4:5] op_sel_hi:[1,0]
	v_pk_add_f32 v[16:17], v[16:17], v[32:33]
	v_pk_add_f32 v[18:19], v[18:19], v[34:35]
	v_pk_mul_f32 v[16:17], v[16:17], s[4:5] op_sel_hi:[1,0]
	v_pk_mul_f32 v[18:19], v[18:19], s[4:5] op_sel_hi:[1,0]
	v_pk_add_f32 v[20:21], v[20:21], v[192:193]
	v_pk_add_f32 v[22:23], v[22:23], v[194:195]
	v_pk_mul_f32 v[20:21], v[20:21], s[4:5] op_sel_hi:[1,0]
	v_pk_mul_f32 v[22:23], v[22:23], s[4:5] op_sel_hi:[1,0]
	global_load_dwordx4 v[24:27], v179, s[46:47] offset:64
	global_load_dwordx4 v[28:31], v180, s[46:47]
	global_load_dwordx4 v[32:35], v180, s[46:47] offset:64
	global_load_dwordx4 v[192:195], v181, s[46:47]
	s_waitcnt vmcnt(10)
	v_pk_fma_f32 v[162:163], v[162:163], v[8:9], v[196:197]
	v_pk_fma_f32 v[164:165], v[164:165], v[10:11], v[198:199]
	v_lshrrev_b32_e32 v187, 1, v176
	v_cvt_pk_bf16_f32 v162, v162, v163
	v_cvt_pk_bf16_f32 v163, v164, v165
	global_store_dwordx2 v187, v[162:163], s[48:49]
	global_load_dwordx4 v[196:199], v181, s[46:47] offset:64
	global_load_dwordx4 v[162:165], v182, s[46:47]
	s_waitcnt vmcnt(12)
	v_pk_fma_f32 v[130:131], v[130:131], v[12:13], v[216:217]
	v_pk_fma_f32 v[132:133], v[132:133], v[14:15], v[218:219]
	v_lshrrev_b32_e32 v172, 1, v176
	v_cvt_pk_bf16_f32 v130, v130, v131
	v_cvt_pk_bf16_f32 v131, v132, v133
	global_store_dwordx2 v172, v[130:131], s[48:49] offset:32
	global_load_dwordx4 v[216:219], v182, s[46:47] offset:64
	global_load_dwordx4 v[130:133], v183, s[46:47]
	s_waitcnt vmcnt(14)
	v_pk_fma_f32 v[158:159], v[158:159], v[8:9], v[220:221]
	v_pk_fma_f32 v[160:161], v[160:161], v[10:11], v[222:223]
	v_lshrrev_b32_e32 v173, 1, v177
	v_cvt_pk_bf16_f32 v158, v158, v159
	v_cvt_pk_bf16_f32 v159, v160, v161
	global_store_dwordx2 v173, v[158:159], s[48:49]
	global_load_dwordx4 v[220:223], v183, s[46:47] offset:64
	global_load_dwordx4 v[158:161], v176, s[46:47] offset:512
	s_waitcnt vmcnt(16)
	v_pk_fma_f32 v[126:127], v[126:127], v[12:13], v[224:225]
	v_pk_fma_f32 v[128:129], v[128:129], v[14:15], v[226:227]
	v_lshrrev_b32_e32 v6, 1, v177
	v_cvt_pk_bf16_f32 v126, v126, v127
	v_cvt_pk_bf16_f32 v127, v128, v129
	global_store_dwordx2 v6, v[126:127], s[48:49] offset:32
	global_load_dwordx4 v[224:227], v176, s[46:47] offset:576
	global_load_dwordx4 v[126:129], v177, s[46:47] offset:512
	s_waitcnt vmcnt(18)
	v_pk_fma_f32 v[154:155], v[154:155], v[8:9], v[228:229]
	v_pk_fma_f32 v[156:157], v[156:157], v[10:11], v[230:231]
	v_lshrrev_b32_e32 v187, 1, v178
	v_cvt_pk_bf16_f32 v154, v154, v155
	v_cvt_pk_bf16_f32 v155, v156, v157
	global_store_dwordx2 v187, v[154:155], s[48:49]
	global_load_dwordx4 v[228:231], v177, s[46:47] offset:576
	global_load_dwordx4 v[154:157], v178, s[46:47] offset:512
	s_waitcnt vmcnt(20)
	v_pk_fma_f32 v[122:123], v[122:123], v[12:13], v[232:233]
	v_pk_fma_f32 v[124:125], v[124:125], v[14:15], v[234:235]
	v_lshrrev_b32_e32 v172, 1, v178
	v_cvt_pk_bf16_f32 v122, v122, v123
	v_cvt_pk_bf16_f32 v123, v124, v125
	global_store_dwordx2 v172, v[122:123], s[48:49] offset:32
	global_load_dwordx4 v[232:235], v178, s[46:47] offset:576
	global_load_dwordx4 v[122:125], v179, s[46:47] offset:512
	s_waitcnt vmcnt(22)
	v_pk_fma_f32 v[150:151], v[150:151], v[8:9], v[236:237]
	v_pk_fma_f32 v[152:153], v[152:153], v[10:11], v[238:239]
	v_lshrrev_b32_e32 v173, 1, v179
	v_cvt_pk_bf16_f32 v150, v150, v151
	v_cvt_pk_bf16_f32 v151, v152, v153
	global_store_dwordx2 v173, v[150:151], s[48:49]
	global_load_dwordx4 v[236:239], v179, s[46:47] offset:576
	global_load_dwordx4 v[150:153], v180, s[46:47] offset:512
	s_waitcnt vmcnt(24)
	v_pk_fma_f32 v[118:119], v[118:119], v[12:13], v[24:25]
	v_pk_fma_f32 v[120:121], v[120:121], v[14:15], v[26:27]
	v_lshrrev_b32_e32 v6, 1, v179
	v_cvt_pk_bf16_f32 v118, v118, v119
	v_cvt_pk_bf16_f32 v119, v120, v121
	global_store_dwordx2 v6, v[118:119], s[48:49] offset:32
	global_load_dwordx4 v[24:27], v180, s[46:47] offset:576
	global_load_dwordx4 v[118:121], v181, s[46:47] offset:512
	s_waitcnt vmcnt(26)
	v_pk_fma_f32 v[146:147], v[146:147], v[8:9], v[28:29]
	v_pk_fma_f32 v[148:149], v[148:149], v[10:11], v[30:31]
	v_lshrrev_b32_e32 v187, 1, v180
	v_cvt_pk_bf16_f32 v146, v146, v147
	v_cvt_pk_bf16_f32 v147, v148, v149
	global_store_dwordx2 v187, v[146:147], s[48:49]
	global_load_dwordx4 v[28:31], v181, s[46:47] offset:576
	global_load_dwordx4 v[146:149], v182, s[46:47] offset:512
	s_waitcnt vmcnt(28)
	v_pk_fma_f32 v[114:115], v[114:115], v[12:13], v[32:33]
	v_pk_fma_f32 v[116:117], v[116:117], v[14:15], v[34:35]
	v_lshrrev_b32_e32 v172, 1, v180
	v_cvt_pk_bf16_f32 v114, v114, v115
	v_cvt_pk_bf16_f32 v115, v116, v117
	global_store_dwordx2 v172, v[114:115], s[48:49] offset:32
	global_load_dwordx4 v[32:35], v182, s[46:47] offset:576
	global_load_dwordx4 v[114:117], v183, s[46:47] offset:512
	s_waitcnt vmcnt(30)
	v_pk_fma_f32 v[142:143], v[142:143], v[8:9], v[192:193]
	v_pk_fma_f32 v[144:145], v[144:145], v[10:11], v[194:195]
	v_lshrrev_b32_e32 v173, 1, v181
	v_cvt_pk_bf16_f32 v142, v142, v143
	v_cvt_pk_bf16_f32 v143, v144, v145
	global_store_dwordx2 v173, v[142:143], s[48:49]
	global_load_dwordx4 v[192:195], v183, s[46:47] offset:576
	s_waitcnt vmcnt(30)
	v_pk_fma_f32 v[110:111], v[110:111], v[12:13], v[196:197]
	v_pk_fma_f32 v[112:113], v[112:113], v[14:15], v[198:199]
	v_lshrrev_b32_e32 v6, 1, v181
	v_cvt_pk_bf16_f32 v110, v110, v111
	v_cvt_pk_bf16_f32 v111, v112, v113
	global_store_dwordx2 v6, v[110:111], s[48:49] offset:32
	s_waitcnt vmcnt(30)
	v_pk_fma_f32 v[138:139], v[138:139], v[8:9], v[162:163]
	v_pk_fma_f32 v[140:141], v[140:141], v[10:11], v[164:165]
	v_lshrrev_b32_e32 v187, 1, v182
	v_cvt_pk_bf16_f32 v138, v138, v139
	v_cvt_pk_bf16_f32 v139, v140, v141
	global_store_dwordx2 v187, v[138:139], s[48:49]
	s_waitcnt vmcnt(29)
	v_pk_fma_f32 v[106:107], v[106:107], v[12:13], v[216:217]
	v_pk_fma_f32 v[108:109], v[108:109], v[14:15], v[218:219]
	v_lshrrev_b32_e32 v172, 1, v182
	v_cvt_pk_bf16_f32 v106, v106, v107
	v_cvt_pk_bf16_f32 v107, v108, v109
	global_store_dwordx2 v172, v[106:107], s[48:49] offset:32
	s_waitcnt vmcnt(29)
	v_pk_fma_f32 v[134:135], v[134:135], v[8:9], v[130:131]
	v_pk_fma_f32 v[136:137], v[136:137], v[10:11], v[132:133]
	v_lshrrev_b32_e32 v173, 1, v183
	v_cvt_pk_bf16_f32 v134, v134, v135
	v_cvt_pk_bf16_f32 v135, v136, v137
	global_store_dwordx2 v173, v[134:135], s[48:49]
	s_waitcnt vmcnt(28)
	v_pk_fma_f32 v[102:103], v[102:103], v[12:13], v[220:221]
	v_pk_fma_f32 v[104:105], v[104:105], v[14:15], v[222:223]
	v_lshrrev_b32_e32 v6, 1, v183
	v_cvt_pk_bf16_f32 v102, v102, v103
	v_cvt_pk_bf16_f32 v103, v104, v105
	global_store_dwordx2 v6, v[102:103], s[48:49] offset:32
	s_waitcnt vmcnt(28)
	v_pk_fma_f32 v[98:99], v[98:99], v[16:17], v[158:159]
	v_pk_fma_f32 v[100:101], v[100:101], v[18:19], v[160:161]
	v_lshrrev_b32_e32 v187, 1, v176
	v_cvt_pk_bf16_f32 v98, v98, v99
	v_cvt_pk_bf16_f32 v99, v100, v101
	global_store_dwordx2 v187, v[98:99], s[48:49] offset:256
	s_waitcnt vmcnt(27)
	v_pk_fma_f32 v[66:67], v[66:67], v[20:21], v[224:225]
	v_pk_fma_f32 v[68:69], v[68:69], v[22:23], v[226:227]
	v_lshrrev_b32_e32 v172, 1, v176
	v_cvt_pk_bf16_f32 v66, v66, v67
	v_cvt_pk_bf16_f32 v67, v68, v69
	global_store_dwordx2 v172, v[66:67], s[48:49] offset:288
	s_waitcnt vmcnt(27)
	v_pk_fma_f32 v[94:95], v[94:95], v[16:17], v[126:127]
	v_pk_fma_f32 v[96:97], v[96:97], v[18:19], v[128:129]
	v_lshrrev_b32_e32 v173, 1, v177
	v_cvt_pk_bf16_f32 v94, v94, v95
	v_cvt_pk_bf16_f32 v95, v96, v97
	global_store_dwordx2 v173, v[94:95], s[48:49] offset:256
	s_waitcnt vmcnt(26)
	v_pk_fma_f32 v[62:63], v[62:63], v[20:21], v[228:229]
	v_pk_fma_f32 v[64:65], v[64:65], v[22:23], v[230:231]
	v_lshrrev_b32_e32 v6, 1, v177
	v_cvt_pk_bf16_f32 v62, v62, v63
	v_cvt_pk_bf16_f32 v63, v64, v65
	global_store_dwordx2 v6, v[62:63], s[48:49] offset:288
	s_waitcnt vmcnt(26)
	v_pk_fma_f32 v[90:91], v[90:91], v[16:17], v[154:155]
	v_pk_fma_f32 v[92:93], v[92:93], v[18:19], v[156:157]
	v_lshrrev_b32_e32 v187, 1, v178
	v_cvt_pk_bf16_f32 v90, v90, v91
	v_cvt_pk_bf16_f32 v91, v92, v93
	global_store_dwordx2 v187, v[90:91], s[48:49] offset:256
	s_waitcnt vmcnt(25)
	v_pk_fma_f32 v[58:59], v[58:59], v[20:21], v[232:233]
	v_pk_fma_f32 v[60:61], v[60:61], v[22:23], v[234:235]
	v_lshrrev_b32_e32 v172, 1, v178
	v_cvt_pk_bf16_f32 v58, v58, v59
	v_cvt_pk_bf16_f32 v59, v60, v61
	global_store_dwordx2 v172, v[58:59], s[48:49] offset:288
	s_waitcnt vmcnt(25)
	v_pk_fma_f32 v[86:87], v[86:87], v[16:17], v[122:123]
	v_pk_fma_f32 v[88:89], v[88:89], v[18:19], v[124:125]
	v_lshrrev_b32_e32 v173, 1, v179
	v_cvt_pk_bf16_f32 v86, v86, v87
	v_cvt_pk_bf16_f32 v87, v88, v89
	global_store_dwordx2 v173, v[86:87], s[48:49] offset:256
	s_waitcnt vmcnt(24)
	v_pk_fma_f32 v[54:55], v[54:55], v[20:21], v[236:237]
	v_pk_fma_f32 v[56:57], v[56:57], v[22:23], v[238:239]
	v_lshrrev_b32_e32 v6, 1, v179
	v_cvt_pk_bf16_f32 v54, v54, v55
	v_cvt_pk_bf16_f32 v55, v56, v57
	global_store_dwordx2 v6, v[54:55], s[48:49] offset:288
	s_waitcnt vmcnt(24)
	v_pk_fma_f32 v[82:83], v[82:83], v[16:17], v[150:151]
	v_pk_fma_f32 v[84:85], v[84:85], v[18:19], v[152:153]
	v_lshrrev_b32_e32 v187, 1, v180
	v_cvt_pk_bf16_f32 v82, v82, v83
	v_cvt_pk_bf16_f32 v83, v84, v85
	global_store_dwordx2 v187, v[82:83], s[48:49] offset:256
	s_waitcnt vmcnt(23)
	v_pk_fma_f32 v[50:51], v[50:51], v[20:21], v[24:25]
	v_pk_fma_f32 v[52:53], v[52:53], v[22:23], v[26:27]
	v_lshrrev_b32_e32 v172, 1, v180
	v_cvt_pk_bf16_f32 v50, v50, v51
	v_cvt_pk_bf16_f32 v51, v52, v53
	global_store_dwordx2 v172, v[50:51], s[48:49] offset:288
	s_waitcnt vmcnt(23)
	v_pk_fma_f32 v[78:79], v[78:79], v[16:17], v[118:119]
	v_pk_fma_f32 v[80:81], v[80:81], v[18:19], v[120:121]
	v_lshrrev_b32_e32 v173, 1, v181
	v_cvt_pk_bf16_f32 v78, v78, v79
	v_cvt_pk_bf16_f32 v79, v80, v81
	global_store_dwordx2 v173, v[78:79], s[48:49] offset:256
	s_waitcnt vmcnt(22)
	v_pk_fma_f32 v[46:47], v[46:47], v[20:21], v[28:29]
	v_pk_fma_f32 v[48:49], v[48:49], v[22:23], v[30:31]
	v_lshrrev_b32_e32 v6, 1, v181
	v_cvt_pk_bf16_f32 v46, v46, v47
	v_cvt_pk_bf16_f32 v47, v48, v49
	global_store_dwordx2 v6, v[46:47], s[48:49] offset:288
	s_waitcnt vmcnt(22)
	v_pk_fma_f32 v[74:75], v[74:75], v[16:17], v[146:147]
	v_pk_fma_f32 v[76:77], v[76:77], v[18:19], v[148:149]
	v_lshrrev_b32_e32 v187, 1, v182
	v_cvt_pk_bf16_f32 v74, v74, v75
	v_cvt_pk_bf16_f32 v75, v76, v77
	global_store_dwordx2 v187, v[74:75], s[48:49] offset:256
	s_waitcnt vmcnt(21)
	v_pk_fma_f32 v[42:43], v[42:43], v[20:21], v[32:33]
	v_pk_fma_f32 v[44:45], v[44:45], v[22:23], v[34:35]
	v_lshrrev_b32_e32 v172, 1, v182
	v_cvt_pk_bf16_f32 v42, v42, v43
	v_cvt_pk_bf16_f32 v43, v44, v45
	global_store_dwordx2 v172, v[42:43], s[48:49] offset:288
	s_waitcnt vmcnt(21)
	v_pk_fma_f32 v[70:71], v[70:71], v[16:17], v[114:115]
	v_pk_fma_f32 v[72:73], v[72:73], v[18:19], v[116:117]
	v_lshrrev_b32_e32 v173, 1, v183
	v_cvt_pk_bf16_f32 v70, v70, v71
	v_cvt_pk_bf16_f32 v71, v72, v73
	global_store_dwordx2 v173, v[70:71], s[48:49] offset:256
	s_waitcnt vmcnt(20)
	v_pk_fma_f32 v[38:39], v[38:39], v[20:21], v[192:193]
	v_pk_fma_f32 v[40:41], v[40:41], v[22:23], v[194:195]
	v_lshrrev_b32_e32 v6, 1, v183
	v_cvt_pk_bf16_f32 v38, v38, v39
	v_cvt_pk_bf16_f32 v39, v40, v41
	global_store_dwordx2 v6, v[38:39], s[48:49] offset:288
	s_andn2_b64 vcc, exec, s[40:41]
	s_cbranch_vccnz .LBB0_691
	v_readlane_b32 s4, v255, 49
	v_readlane_b32 s5, v255, 50
	s_andn2_b64 vcc, exec, s[4:5]
	s_cbranch_vccnz .LBB0_690
	s_barrier
	s_branch .LBB0_690
